# 36 K-loop LDS-DMA pieces use the scalar-base form (global_load_lds_dwordx4 vOffset, s[base]) instead of a 64-bit VALU add into a temporary; on top of v90
# speedup vs baseline: 1.0121x; 1.0027x over previous
.Lp1_blk3:
	ds_read_b128 v[184:187], v175 offset:32768
	ds_read_b128 v[188:191], v176 offset:32768
	ds_read_b128 v[192:195], v175 offset:34816
	ds_read_b128 v[196:199], v176 offset:34816
	ds_read_b128 v[200:203], v175 offset:49152
	ds_read_b128 v[204:207], v176 offset:49152
	ds_read_b128 v[208:211], v175 offset:51200
	ds_read_b128 v[212:215], v176 offset:51200
	s_mov_b32 m0, s77
	ds_read_b128 v[216:219], v178 offset:32768
	ds_read_b128 v[220:223], v178 offset:34816
	ds_read_b128 v[224:227], v179 offset:32768
	ds_read_b128 v[228:231], v179 offset:34816
	ds_read_b128 v[232:235], v178 offset:36864
	ds_read_b128 v[236:239], v178 offset:38912
	ds_read_b128 v[240:243], v179 offset:36864
	ds_read_b128 v[244:247], v179 offset:38912
	global_load_lds_dwordx4 v166, s[70:71]
	s_mov_b32 m0, s78
	global_load_lds_dwordx4 v164, s[70:71]
	s_mov_b32 m0, s79
	global_load_lds_dwordx4 v162, s[70:71]
	s_mov_b32 m0, s80
	s_nop 0
	global_load_lds_dwordx4 v160, s[70:71]
	s_waitcnt vmcnt(8)
	s_waitcnt lgkmcnt(0)
	s_barrier
	s_setprio 1
	s_waitcnt lgkmcnt(0)
	v_mfma_f32_16x16x32_bf16 v[126:129], v[184:187], v[216:219], v[126:129]
	v_mfma_f32_16x16x32_bf16 v[122:125], v[192:195], v[216:219], v[122:125]
	v_mfma_f32_16x16x32_bf16 v[118:121], v[184:187], v[220:223], v[118:121]
	v_mfma_f32_16x16x32_bf16 v[114:117], v[192:195], v[220:223], v[114:117]
	v_mfma_f32_16x16x32_bf16 v[110:113], v[184:187], v[232:235], v[110:113]
	v_mfma_f32_16x16x32_bf16 v[106:109], v[192:195], v[232:235], v[106:109]
	v_mfma_f32_16x16x32_bf16 v[102:105], v[184:187], v[236:239], v[102:105]
	v_mfma_f32_16x16x32_bf16 v[98:101], v[192:195], v[236:239], v[98:101]
	v_mfma_f32_16x16x32_bf16 v[126:129], v[188:191], v[224:227], v[126:129]
	v_mfma_f32_16x16x32_bf16 v[122:125], v[196:199], v[224:227], v[122:125]
	v_mfma_f32_16x16x32_bf16 v[118:121], v[188:191], v[228:231], v[118:121]
	v_mfma_f32_16x16x32_bf16 v[114:117], v[196:199], v[228:231], v[114:117]
	v_mfma_f32_16x16x32_bf16 v[110:113], v[188:191], v[240:243], v[110:113]
	v_mfma_f32_16x16x32_bf16 v[106:109], v[196:199], v[240:243], v[106:109]
	v_mfma_f32_16x16x32_bf16 v[102:105], v[188:191], v[244:247], v[102:105]
	v_mfma_f32_16x16x32_bf16 v[98:101], v[196:199], v[244:247], v[98:101]
	s_setprio 0
	s_setprio 1
	v_mfma_f32_16x16x32_bf16 v[62:65], v[200:203], v[216:219], v[62:65]
	v_mfma_f32_16x16x32_bf16 v[58:61], v[208:211], v[216:219], v[58:61]
	v_mfma_f32_16x16x32_bf16 v[54:57], v[200:203], v[220:223], v[54:57]
	v_mfma_f32_16x16x32_bf16 v[50:53], v[208:211], v[220:223], v[50:53]
	v_mfma_f32_16x16x32_bf16 v[46:49], v[200:203], v[232:235], v[46:49]
	v_mfma_f32_16x16x32_bf16 v[42:45], v[208:211], v[232:235], v[42:45]
	v_mfma_f32_16x16x32_bf16 v[38:41], v[200:203], v[236:239], v[38:41]
	v_mfma_f32_16x16x32_bf16 v[34:37], v[208:211], v[236:239], v[34:37]
	v_mfma_f32_16x16x32_bf16 v[62:65], v[204:207], v[224:227], v[62:65]
	v_mfma_f32_16x16x32_bf16 v[58:61], v[212:215], v[224:227], v[58:61]
	v_mfma_f32_16x16x32_bf16 v[54:57], v[204:207], v[228:231], v[54:57]
	v_mfma_f32_16x16x32_bf16 v[50:53], v[212:215], v[228:231], v[50:53]
	v_mfma_f32_16x16x32_bf16 v[46:49], v[204:207], v[240:243], v[46:49]
	v_mfma_f32_16x16x32_bf16 v[42:45], v[212:215], v[240:243], v[42:45]
	v_mfma_f32_16x16x32_bf16 v[38:41], v[204:207], v[244:247], v[38:41]
	v_mfma_f32_16x16x32_bf16 v[34:37], v[212:215], v[244:247], v[34:37]
	s_setprio 0
	s_barrier
	s_add_i32 s70, s92, s76
	v_lshl_add_u64 v[240:241], v[248:249], 0, s[8:9]
	s_mov_b32 m0, s70
	ds_read_b128 v[160:163], v178 offset:49152
	ds_read_b128 v[164:167], v178 offset:51200
	ds_read_b128 v[216:219], v179 offset:49152
	ds_read_b128 v[220:223], v179 offset:51200
	ds_read_b128 v[224:227], v178 offset:53248
	ds_read_b128 v[228:231], v178 offset:55296
	ds_read_b128 v[232:235], v179 offset:53248
	ds_read_b128 v[236:239], v179 offset:55296
	global_load_lds_dwordx4 v[240:241], off
	s_add_i32 m0, s70, 0x2000
	s_add_u32 s68, s68, 0x80080
	v_lshl_add_u64 v[240:241], v[250:251], 0, s[8:9]
	s_addc_u32 s69, s69, 0
	s_add_i32 s70, s94, s76
	global_load_lds_dwordx4 v[240:241], off
	s_mov_b32 m0, s70
	s_nop 0
	global_load_lds_dwordx4 v142, s[68:69]
	s_add_i32 m0, s70, 0x2000
	s_nop 0
	global_load_lds_dwordx4 v144, s[68:69]
	s_waitcnt vmcnt(6)
	s_waitcnt lgkmcnt(0)
	s_barrier
	s_setprio 1
	s_waitcnt lgkmcnt(0)
	v_mfma_f32_16x16x32_bf16 v[94:97], v[184:187], v[160:163], v[94:97]
	v_mfma_f32_16x16x32_bf16 v[90:93], v[192:195], v[160:163], v[90:93]
	v_mfma_f32_16x16x32_bf16 v[86:89], v[184:187], v[164:167], v[86:89]
	v_mfma_f32_16x16x32_bf16 v[82:85], v[192:195], v[164:167], v[82:85]
	v_mfma_f32_16x16x32_bf16 v[78:81], v[184:187], v[224:227], v[78:81]
	v_mfma_f32_16x16x32_bf16 v[74:77], v[192:195], v[224:227], v[74:77]
	v_mfma_f32_16x16x32_bf16 v[70:73], v[184:187], v[228:231], v[70:73]
	v_mfma_f32_16x16x32_bf16 v[66:69], v[192:195], v[228:231], v[66:69]
	v_mfma_f32_16x16x32_bf16 v[94:97], v[188:191], v[216:219], v[94:97]
	v_mfma_f32_16x16x32_bf16 v[90:93], v[196:199], v[216:219], v[90:93]
	v_mfma_f32_16x16x32_bf16 v[86:89], v[188:191], v[220:223], v[86:89]
	v_mfma_f32_16x16x32_bf16 v[82:85], v[196:199], v[220:223], v[82:85]
	v_mfma_f32_16x16x32_bf16 v[78:81], v[188:191], v[232:235], v[78:81]
	v_mfma_f32_16x16x32_bf16 v[74:77], v[196:199], v[232:235], v[74:77]
	v_mfma_f32_16x16x32_bf16 v[70:73], v[188:191], v[236:239], v[70:73]
	v_mfma_f32_16x16x32_bf16 v[66:69], v[196:199], v[236:239], v[66:69]
	s_setprio 0
	s_setprio 1
	v_mfma_f32_16x16x32_bf16 v[30:33], v[200:203], v[160:163], v[30:33]
	v_mfma_f32_16x16x32_bf16 v[26:29], v[208:211], v[160:163], v[26:29]
	v_mfma_f32_16x16x32_bf16 v[22:25], v[200:203], v[164:167], v[22:25]
	v_mfma_f32_16x16x32_bf16 v[18:21], v[208:211], v[164:167], v[18:21]
	v_mfma_f32_16x16x32_bf16 v[14:17], v[200:203], v[224:227], v[14:17]
	v_mfma_f32_16x16x32_bf16 v[10:13], v[208:211], v[224:227], v[10:13]
	v_mfma_f32_16x16x32_bf16 v[6:9], v[200:203], v[228:231], v[6:9]
	v_mfma_f32_16x16x32_bf16 v[2:5], v[208:211], v[228:231], v[2:5]
	v_mfma_f32_16x16x32_bf16 v[30:33], v[204:207], v[216:219], v[30:33]
	v_mfma_f32_16x16x32_bf16 v[26:29], v[212:215], v[216:219], v[26:29]
	v_mfma_f32_16x16x32_bf16 v[22:25], v[204:207], v[220:223], v[22:25]
	v_mfma_f32_16x16x32_bf16 v[18:21], v[212:215], v[220:223], v[18:21]
	v_mfma_f32_16x16x32_bf16 v[14:17], v[204:207], v[232:235], v[14:17]
	v_mfma_f32_16x16x32_bf16 v[10:13], v[212:215], v[232:235], v[10:13]
	v_mfma_f32_16x16x32_bf16 v[6:9], v[204:207], v[236:239], v[6:9]
	v_mfma_f32_16x16x32_bf16 v[2:5], v[212:215], v[236:239], v[2:5]
	s_setprio 0
	s_barrier
	s_add_i32 s72, s72, 2
	s_add_u32 s66, s66, 0x100
	s_addc_u32 s67, s67, 0
	s_cmp_gt_u32 s72, 29
	s_cbranch_scc1 .LBB0_105

.Lp3_first:
	ds_read_b128 v[184:187], v174
	ds_read_b128 v[188:191], v175
	ds_read_b128 v[192:195], v174 offset:2048
	ds_read_b128 v[196:199], v175 offset:2048
	ds_read_b128 v[200:203], v174 offset:16384
	ds_read_b128 v[204:207], v175 offset:16384
	ds_read_b128 v[208:211], v174 offset:18432
	ds_read_b128 v[212:215], v175 offset:18432
	v_lshl_add_u64 v[248:249], v[158:159], 0, s[28:29]
	s_add_i32 m0, s39, 0x8000
	ds_read_b128 v[216:219], v177
	ds_read_b128 v[220:223], v177 offset:2048
	ds_read_b128 v[224:227], v178
	ds_read_b128 v[228:231], v178 offset:2048
	ds_read_b128 v[232:235], v177 offset:4096
	ds_read_b128 v[236:239], v177 offset:6144
	ds_read_b128 v[240:243], v178 offset:4096
	ds_read_b128 v[244:247], v178 offset:6144
	global_load_lds_dwordx4 v[248:249], off
	v_lshl_add_u64 v[248:249], v[156:157], 0, s[28:29]
	s_add_i32 m0, s39, 0xa000
	s_nop 0
	global_load_lds_dwordx4 v[248:249], off
	v_lshl_add_u64 v[248:249], v[154:155], 0, s[28:29]
	s_add_i32 m0, s39, 0xc000
	s_nop 0
	global_load_lds_dwordx4 v[248:249], off
	v_lshl_add_u64 v[248:249], v[144:145], 0, s[28:29]
	s_add_i32 m0, s39, 0xe000
	s_nop 0
	global_load_lds_dwordx4 v[248:249], off
	s_waitcnt vmcnt(8)
	s_waitcnt lgkmcnt(0)
	s_barrier
	s_setprio 1
	s_waitcnt lgkmcnt(0)
	v_mfma_f32_16x16x32_bf16 v[126:129], v[184:187], v[216:219], 0
	s_add_u32 s34, s2, s28
	s_addc_u32 s35, s3, s29
	s_add_u32 s77, s34, 0x63000100
	s_addc_u32 s78, s35, 0
	v_mfma_f32_16x16x32_bf16 v[122:125], v[192:195], v[216:219], 0
	s_and_b64 s[34:35], s[30:31], exec
	s_cselect_b32 s35, s7, s78
	s_cselect_b32 s34, s6, s77
	s_add_u32 s77, s25, s28
	v_mfma_f32_16x16x32_bf16 v[118:121], v[184:187], v[220:223], 0
	s_addc_u32 s78, s75, s29
	s_and_b64 s[30:31], s[30:31], exec
	s_cselect_b32 s31, s27, s78
	s_cselect_b32 s30, s26, s77
	v_mfma_f32_16x16x32_bf16 v[114:117], v[192:195], v[220:223], 0
	v_mfma_f32_16x16x32_bf16 v[110:113], v[184:187], v[232:235], 0
	v_mfma_f32_16x16x32_bf16 v[102:105], v[192:195], v[232:235], 0
	v_mfma_f32_16x16x32_bf16 v[94:97], v[184:187], v[236:239], 0
	v_mfma_f32_16x16x32_bf16 v[86:89], v[192:195], v[236:239], 0
	v_mfma_f32_16x16x32_bf16 v[126:129], v[188:191], v[224:227], v[126:129]
	v_mfma_f32_16x16x32_bf16 v[122:125], v[196:199], v[224:227], v[122:125]
	v_mfma_f32_16x16x32_bf16 v[118:121], v[188:191], v[228:231], v[118:121]
	v_mfma_f32_16x16x32_bf16 v[114:117], v[196:199], v[228:231], v[114:117]
	v_mfma_f32_16x16x32_bf16 v[110:113], v[188:191], v[240:243], v[110:113]
	v_mfma_f32_16x16x32_bf16 v[102:105], v[196:199], v[240:243], v[102:105]
	v_mfma_f32_16x16x32_bf16 v[94:97], v[188:191], v[244:247], v[94:97]
	v_mfma_f32_16x16x32_bf16 v[86:89], v[196:199], v[244:247], v[86:89]
	s_setprio 0
	s_setprio 1
	v_mfma_f32_16x16x32_bf16 v[106:109], v[200:203], v[216:219], 0
	v_mfma_f32_16x16x32_bf16 v[98:101], v[208:211], v[216:219], 0
	v_mfma_f32_16x16x32_bf16 v[90:93], v[200:203], v[220:223], 0
	v_mfma_f32_16x16x32_bf16 v[82:85], v[208:211], v[220:223], 0
	v_mfma_f32_16x16x32_bf16 v[78:81], v[200:203], v[232:235], 0
	v_mfma_f32_16x16x32_bf16 v[74:77], v[208:211], v[232:235], 0
	v_mfma_f32_16x16x32_bf16 v[70:73], v[200:203], v[236:239], 0
	v_mfma_f32_16x16x32_bf16 v[66:69], v[208:211], v[236:239], 0
	v_mfma_f32_16x16x32_bf16 v[106:109], v[204:207], v[224:227], v[106:109]
	v_mfma_f32_16x16x32_bf16 v[98:101], v[212:215], v[224:227], v[98:101]
	v_mfma_f32_16x16x32_bf16 v[90:93], v[204:207], v[228:231], v[90:93]
	v_mfma_f32_16x16x32_bf16 v[82:85], v[212:215], v[228:231], v[82:85]
	v_mfma_f32_16x16x32_bf16 v[78:81], v[204:207], v[240:243], v[78:81]
	v_mfma_f32_16x16x32_bf16 v[74:77], v[212:215], v[240:243], v[74:77]
	v_mfma_f32_16x16x32_bf16 v[70:73], v[204:207], v[244:247], v[70:73]
	v_mfma_f32_16x16x32_bf16 v[66:69], v[212:215], v[244:247], v[66:69]
	s_setprio 0
	s_barrier
	s_add_i32 s77, s45, s33
	v_lshl_add_u64 v[248:249], s[30:31], 0, v[146:147]
	s_mov_b32 m0, s77
	ds_read_b128 v[216:219], v177 offset:16384
	ds_read_b128 v[220:223], v177 offset:18432
	ds_read_b128 v[224:227], v178 offset:16384
	ds_read_b128 v[228:231], v178 offset:18432
	ds_read_b128 v[232:235], v177 offset:20480
	ds_read_b128 v[236:239], v177 offset:22528
	ds_read_b128 v[240:243], v178 offset:20480
	ds_read_b128 v[244:247], v178 offset:22528
	global_load_lds_dwordx4 v[248:249], off
	s_add_i32 m0, s77, 0x2000
	s_add_u32 s78, s30, 0x80000
	v_lshl_add_u64 v[250:251], s[30:31], 0, v[148:149]
	s_addc_u32 s79, s31, 0
	s_add_i32 s77, s47, s33
	global_load_lds_dwordx4 v[250:251], off
	s_mov_b32 m0, s77
	s_nop 0
	global_load_lds_dwordx4 v146, s[78:79]
	s_add_i32 m0, s77, 0x2000
	s_nop 0
	global_load_lds_dwordx4 v148, s[78:79]
	s_waitcnt vmcnt(6)
	s_waitcnt lgkmcnt(0)
	s_barrier
	s_setprio 1
	s_waitcnt lgkmcnt(0)
	v_mfma_f32_16x16x32_bf16 v[62:65], v[184:187], v[216:219], 0
	v_mfma_f32_16x16x32_bf16 v[58:61], v[192:195], v[216:219], 0
	v_mfma_f32_16x16x32_bf16 v[50:53], v[184:187], v[220:223], 0
	v_mfma_f32_16x16x32_bf16 v[42:45], v[192:195], v[220:223], 0
	v_mfma_f32_16x16x32_bf16 v[34:37], v[184:187], v[232:235], 0
	v_mfma_f32_16x16x32_bf16 v[26:29], v[192:195], v[232:235], 0
	v_mfma_f32_16x16x32_bf16 v[18:21], v[184:187], v[236:239], 0
	v_mfma_f32_16x16x32_bf16 v[10:13], v[192:195], v[236:239], 0
	v_mfma_f32_16x16x32_bf16 v[62:65], v[188:191], v[224:227], v[62:65]
	v_mfma_f32_16x16x32_bf16 v[58:61], v[196:199], v[224:227], v[58:61]
	v_mfma_f32_16x16x32_bf16 v[50:53], v[188:191], v[228:231], v[50:53]
	v_mfma_f32_16x16x32_bf16 v[42:45], v[196:199], v[228:231], v[42:45]
	v_mfma_f32_16x16x32_bf16 v[34:37], v[188:191], v[240:243], v[34:37]
	v_mfma_f32_16x16x32_bf16 v[26:29], v[196:199], v[240:243], v[26:29]
	v_mfma_f32_16x16x32_bf16 v[18:21], v[188:191], v[244:247], v[18:21]
	v_mfma_f32_16x16x32_bf16 v[10:13], v[196:199], v[244:247], v[10:13]
	s_setprio 0
	s_setprio 1
	v_mfma_f32_16x16x32_bf16 v[54:57], v[200:203], v[216:219], 0
	v_mfma_f32_16x16x32_bf16 v[46:49], v[208:211], v[216:219], 0
	v_mfma_f32_16x16x32_bf16 v[38:41], v[200:203], v[220:223], 0
	v_mfma_f32_16x16x32_bf16 v[30:33], v[208:211], v[220:223], 0
	v_mfma_f32_16x16x32_bf16 v[22:25], v[200:203], v[232:235], 0
	v_mfma_f32_16x16x32_bf16 v[14:17], v[208:211], v[232:235], 0
	v_mfma_f32_16x16x32_bf16 v[6:9], v[200:203], v[236:239], 0
	v_mfma_f32_16x16x32_bf16 v[2:5], v[208:211], v[236:239], 0
	v_mfma_f32_16x16x32_bf16 v[54:57], v[204:207], v[224:227], v[54:57]
	v_mfma_f32_16x16x32_bf16 v[46:49], v[212:215], v[224:227], v[46:49]
	v_mfma_f32_16x16x32_bf16 v[38:41], v[204:207], v[228:231], v[38:41]
	v_mfma_f32_16x16x32_bf16 v[30:33], v[212:215], v[228:231], v[30:33]
	v_mfma_f32_16x16x32_bf16 v[22:25], v[204:207], v[240:243], v[22:25]
	v_mfma_f32_16x16x32_bf16 v[14:17], v[212:215], v[240:243], v[14:17]
	v_mfma_f32_16x16x32_bf16 v[6:9], v[204:207], v[244:247], v[6:9]
	v_mfma_f32_16x16x32_bf16 v[2:5], v[212:215], v[244:247], v[2:5]
	s_setprio 0
	s_barrier
	s_branch .Lp3_blk3

.LBB0_385:
	s_cmp_eq_u32 s28, 0
	s_cbranch_scc1 .Lp3_first
	ds_read_b128 v[184:187], v174
	ds_read_b128 v[188:191], v175
	ds_read_b128 v[192:195], v174 offset:2048
	ds_read_b128 v[196:199], v175 offset:2048
	ds_read_b128 v[200:203], v174 offset:16384
	ds_read_b128 v[204:207], v175 offset:16384
	ds_read_b128 v[208:211], v174 offset:18432
	ds_read_b128 v[212:215], v175 offset:18432
	v_lshl_add_u64 v[248:249], v[158:159], 0, s[28:29]
	s_add_i32 m0, s39, 0x8000
	ds_read_b128 v[216:219], v177
	ds_read_b128 v[220:223], v177 offset:2048
	ds_read_b128 v[224:227], v178
	ds_read_b128 v[228:231], v178 offset:2048
	ds_read_b128 v[232:235], v177 offset:4096
	ds_read_b128 v[236:239], v177 offset:6144
	ds_read_b128 v[240:243], v178 offset:4096
	ds_read_b128 v[244:247], v178 offset:6144
	global_load_lds_dwordx4 v[248:249], off
	v_lshl_add_u64 v[248:249], v[156:157], 0, s[28:29]
	s_add_i32 m0, s39, 0xa000
	s_nop 0
	global_load_lds_dwordx4 v[248:249], off
	v_lshl_add_u64 v[248:249], v[154:155], 0, s[28:29]
	s_add_i32 m0, s39, 0xc000
	s_nop 0
	global_load_lds_dwordx4 v[248:249], off
	v_lshl_add_u64 v[248:249], v[144:145], 0, s[28:29]
	s_add_i32 m0, s39, 0xe000
	s_nop 0
	global_load_lds_dwordx4 v[248:249], off
	s_waitcnt vmcnt(8)
	s_waitcnt lgkmcnt(0)
	s_barrier
	s_setprio 1
	s_waitcnt lgkmcnt(0)
	v_mfma_f32_16x16x32_bf16 v[126:129], v[184:187], v[216:219], v[126:129]
	s_add_u32 s34, s2, s28
	s_addc_u32 s35, s3, s29
	s_add_u32 s77, s34, 0x63000100
	s_addc_u32 s78, s35, 0
	v_mfma_f32_16x16x32_bf16 v[122:125], v[192:195], v[216:219], v[122:125]
	s_and_b64 s[34:35], s[30:31], exec
	s_cselect_b32 s35, s7, s78
	s_cselect_b32 s34, s6, s77
	s_add_u32 s77, s25, s28
	v_mfma_f32_16x16x32_bf16 v[118:121], v[184:187], v[220:223], v[118:121]
	s_addc_u32 s78, s75, s29
	s_and_b64 s[30:31], s[30:31], exec
	s_cselect_b32 s31, s27, s78
	s_cselect_b32 s30, s26, s77
	v_mfma_f32_16x16x32_bf16 v[114:117], v[192:195], v[220:223], v[114:117]
	v_mfma_f32_16x16x32_bf16 v[110:113], v[184:187], v[232:235], v[110:113]
	v_mfma_f32_16x16x32_bf16 v[102:105], v[192:195], v[232:235], v[102:105]
	v_mfma_f32_16x16x32_bf16 v[94:97], v[184:187], v[236:239], v[94:97]
	v_mfma_f32_16x16x32_bf16 v[86:89], v[192:195], v[236:239], v[86:89]
	v_mfma_f32_16x16x32_bf16 v[126:129], v[188:191], v[224:227], v[126:129]
	v_mfma_f32_16x16x32_bf16 v[122:125], v[196:199], v[224:227], v[122:125]
	v_mfma_f32_16x16x32_bf16 v[118:121], v[188:191], v[228:231], v[118:121]
	v_mfma_f32_16x16x32_bf16 v[114:117], v[196:199], v[228:231], v[114:117]
	v_mfma_f32_16x16x32_bf16 v[110:113], v[188:191], v[240:243], v[110:113]
	v_mfma_f32_16x16x32_bf16 v[102:105], v[196:199], v[240:243], v[102:105]
	v_mfma_f32_16x16x32_bf16 v[94:97], v[188:191], v[244:247], v[94:97]
	v_mfma_f32_16x16x32_bf16 v[86:89], v[196:199], v[244:247], v[86:89]
	s_setprio 0
	s_setprio 1
	v_mfma_f32_16x16x32_bf16 v[106:109], v[200:203], v[216:219], v[106:109]
	v_mfma_f32_16x16x32_bf16 v[98:101], v[208:211], v[216:219], v[98:101]
	v_mfma_f32_16x16x32_bf16 v[90:93], v[200:203], v[220:223], v[90:93]
	v_mfma_f32_16x16x32_bf16 v[82:85], v[208:211], v[220:223], v[82:85]
	v_mfma_f32_16x16x32_bf16 v[78:81], v[200:203], v[232:235], v[78:81]
	v_mfma_f32_16x16x32_bf16 v[74:77], v[208:211], v[232:235], v[74:77]
	v_mfma_f32_16x16x32_bf16 v[70:73], v[200:203], v[236:239], v[70:73]
	v_mfma_f32_16x16x32_bf16 v[66:69], v[208:211], v[236:239], v[66:69]
	v_mfma_f32_16x16x32_bf16 v[106:109], v[204:207], v[224:227], v[106:109]
	v_mfma_f32_16x16x32_bf16 v[98:101], v[212:215], v[224:227], v[98:101]
	v_mfma_f32_16x16x32_bf16 v[90:93], v[204:207], v[228:231], v[90:93]
	v_mfma_f32_16x16x32_bf16 v[82:85], v[212:215], v[228:231], v[82:85]
	v_mfma_f32_16x16x32_bf16 v[78:81], v[204:207], v[240:243], v[78:81]
	v_mfma_f32_16x16x32_bf16 v[74:77], v[212:215], v[240:243], v[74:77]
	v_mfma_f32_16x16x32_bf16 v[70:73], v[204:207], v[244:247], v[70:73]
	v_mfma_f32_16x16x32_bf16 v[66:69], v[212:215], v[244:247], v[66:69]
	s_setprio 0
	s_barrier
	s_add_i32 s77, s45, s33
	v_lshl_add_u64 v[248:249], s[30:31], 0, v[146:147]
	s_mov_b32 m0, s77
	ds_read_b128 v[216:219], v177 offset:16384
	ds_read_b128 v[220:223], v177 offset:18432
	ds_read_b128 v[224:227], v178 offset:16384
	ds_read_b128 v[228:231], v178 offset:18432
	ds_read_b128 v[232:235], v177 offset:20480
	ds_read_b128 v[236:239], v177 offset:22528
	ds_read_b128 v[240:243], v178 offset:20480
	ds_read_b128 v[244:247], v178 offset:22528
	global_load_lds_dwordx4 v[248:249], off
	s_add_i32 m0, s77, 0x2000
	s_add_u32 s78, s30, 0x80000
	v_lshl_add_u64 v[250:251], s[30:31], 0, v[148:149]
	s_addc_u32 s79, s31, 0
	s_add_i32 s77, s47, s33
	global_load_lds_dwordx4 v[250:251], off
	s_mov_b32 m0, s77
	s_nop 0
	global_load_lds_dwordx4 v146, s[78:79]
	s_add_i32 m0, s77, 0x2000
	s_nop 0
	global_load_lds_dwordx4 v148, s[78:79]
	s_waitcnt vmcnt(6)
	s_waitcnt lgkmcnt(0)
	s_barrier
	s_setprio 1
	s_waitcnt lgkmcnt(0)
	v_mfma_f32_16x16x32_bf16 v[62:65], v[184:187], v[216:219], v[62:65]
	v_mfma_f32_16x16x32_bf16 v[58:61], v[192:195], v[216:219], v[58:61]
	v_mfma_f32_16x16x32_bf16 v[50:53], v[184:187], v[220:223], v[50:53]
	v_mfma_f32_16x16x32_bf16 v[42:45], v[192:195], v[220:223], v[42:45]
	v_mfma_f32_16x16x32_bf16 v[34:37], v[184:187], v[232:235], v[34:37]
	v_mfma_f32_16x16x32_bf16 v[26:29], v[192:195], v[232:235], v[26:29]
	v_mfma_f32_16x16x32_bf16 v[18:21], v[184:187], v[236:239], v[18:21]
	v_mfma_f32_16x16x32_bf16 v[10:13], v[192:195], v[236:239], v[10:13]
	v_mfma_f32_16x16x32_bf16 v[62:65], v[188:191], v[224:227], v[62:65]
	v_mfma_f32_16x16x32_bf16 v[58:61], v[196:199], v[224:227], v[58:61]
	v_mfma_f32_16x16x32_bf16 v[50:53], v[188:191], v[228:231], v[50:53]
	v_mfma_f32_16x16x32_bf16 v[42:45], v[196:199], v[228:231], v[42:45]
	v_mfma_f32_16x16x32_bf16 v[34:37], v[188:191], v[240:243], v[34:37]
	v_mfma_f32_16x16x32_bf16 v[26:29], v[196:199], v[240:243], v[26:29]
	v_mfma_f32_16x16x32_bf16 v[18:21], v[188:191], v[244:247], v[18:21]
	v_mfma_f32_16x16x32_bf16 v[10:13], v[196:199], v[244:247], v[10:13]
	s_setprio 0
	s_setprio 1
	v_mfma_f32_16x16x32_bf16 v[54:57], v[200:203], v[216:219], v[54:57]
	v_mfma_f32_16x16x32_bf16 v[46:49], v[208:211], v[216:219], v[46:49]
	v_mfma_f32_16x16x32_bf16 v[38:41], v[200:203], v[220:223], v[38:41]
	v_mfma_f32_16x16x32_bf16 v[30:33], v[208:211], v[220:223], v[30:33]
	v_mfma_f32_16x16x32_bf16 v[22:25], v[200:203], v[232:235], v[22:25]
	v_mfma_f32_16x16x32_bf16 v[14:17], v[208:211], v[232:235], v[14:17]
	v_mfma_f32_16x16x32_bf16 v[6:9], v[200:203], v[236:239], v[6:9]
	v_mfma_f32_16x16x32_bf16 v[2:5], v[208:211], v[236:239], v[2:5]
	v_mfma_f32_16x16x32_bf16 v[54:57], v[204:207], v[224:227], v[54:57]
	v_mfma_f32_16x16x32_bf16 v[46:49], v[212:215], v[224:227], v[46:49]
	v_mfma_f32_16x16x32_bf16 v[38:41], v[204:207], v[228:231], v[38:41]
	v_mfma_f32_16x16x32_bf16 v[30:33], v[212:215], v[228:231], v[30:33]
	v_mfma_f32_16x16x32_bf16 v[22:25], v[204:207], v[240:243], v[22:25]
	v_mfma_f32_16x16x32_bf16 v[14:17], v[212:215], v[240:243], v[14:17]
	v_mfma_f32_16x16x32_bf16 v[6:9], v[204:207], v[244:247], v[6:9]
	v_mfma_f32_16x16x32_bf16 v[2:5], v[212:215], v[244:247], v[2:5]
	s_setprio 0
	s_barrier
.Lp3_blk3:
	ds_read_b128 v[184:187], v174 offset:32768
	ds_read_b128 v[188:191], v175 offset:32768
	ds_read_b128 v[192:195], v174 offset:34816
	ds_read_b128 v[196:199], v175 offset:34816
	ds_read_b128 v[200:203], v174 offset:49152
	ds_read_b128 v[204:207], v175 offset:49152
	ds_read_b128 v[208:211], v174 offset:51200
	ds_read_b128 v[212:215], v175 offset:51200
	s_mov_b32 m0, s39
	ds_read_b128 v[216:219], v177 offset:32768
	ds_read_b128 v[220:223], v177 offset:34816
	ds_read_b128 v[224:227], v178 offset:32768
	ds_read_b128 v[228:231], v178 offset:34816
	ds_read_b128 v[232:235], v177 offset:36864
	ds_read_b128 v[236:239], v177 offset:38912
	ds_read_b128 v[240:243], v178 offset:36864
	ds_read_b128 v[244:247], v178 offset:38912
	global_load_lds_dwordx4 v166, s[34:35]
	s_mov_b32 m0, s40
	global_load_lds_dwordx4 v164, s[34:35]
	s_mov_b32 m0, s41
	global_load_lds_dwordx4 v162, s[34:35]
	s_mov_b32 m0, s42
	s_nop 0
	global_load_lds_dwordx4 v160, s[34:35]
	s_waitcnt vmcnt(8)
	s_waitcnt lgkmcnt(0)
	s_barrier
	s_setprio 1
	s_waitcnt lgkmcnt(0)
	v_mfma_f32_16x16x32_bf16 v[126:129], v[184:187], v[216:219], v[126:129]
	v_mfma_f32_16x16x32_bf16 v[122:125], v[192:195], v[216:219], v[122:125]
	v_mfma_f32_16x16x32_bf16 v[118:121], v[184:187], v[220:223], v[118:121]
	v_mfma_f32_16x16x32_bf16 v[114:117], v[192:195], v[220:223], v[114:117]
	v_mfma_f32_16x16x32_bf16 v[110:113], v[184:187], v[232:235], v[110:113]
	v_mfma_f32_16x16x32_bf16 v[102:105], v[192:195], v[232:235], v[102:105]
	v_mfma_f32_16x16x32_bf16 v[94:97], v[184:187], v[236:239], v[94:97]
	v_mfma_f32_16x16x32_bf16 v[86:89], v[192:195], v[236:239], v[86:89]
	v_mfma_f32_16x16x32_bf16 v[126:129], v[188:191], v[224:227], v[126:129]
	v_mfma_f32_16x16x32_bf16 v[122:125], v[196:199], v[224:227], v[122:125]
	v_mfma_f32_16x16x32_bf16 v[118:121], v[188:191], v[228:231], v[118:121]
	v_mfma_f32_16x16x32_bf16 v[114:117], v[196:199], v[228:231], v[114:117]
	v_mfma_f32_16x16x32_bf16 v[110:113], v[188:191], v[240:243], v[110:113]
	v_mfma_f32_16x16x32_bf16 v[102:105], v[196:199], v[240:243], v[102:105]
	v_mfma_f32_16x16x32_bf16 v[94:97], v[188:191], v[244:247], v[94:97]
	v_mfma_f32_16x16x32_bf16 v[86:89], v[196:199], v[244:247], v[86:89]
	s_setprio 0
	s_setprio 1
	v_mfma_f32_16x16x32_bf16 v[106:109], v[200:203], v[216:219], v[106:109]
	v_mfma_f32_16x16x32_bf16 v[98:101], v[208:211], v[216:219], v[98:101]
	v_mfma_f32_16x16x32_bf16 v[90:93], v[200:203], v[220:223], v[90:93]
	v_mfma_f32_16x16x32_bf16 v[82:85], v[208:211], v[220:223], v[82:85]
	v_mfma_f32_16x16x32_bf16 v[78:81], v[200:203], v[232:235], v[78:81]
	v_mfma_f32_16x16x32_bf16 v[74:77], v[208:211], v[232:235], v[74:77]
	v_mfma_f32_16x16x32_bf16 v[70:73], v[200:203], v[236:239], v[70:73]
	v_mfma_f32_16x16x32_bf16 v[66:69], v[208:211], v[236:239], v[66:69]
	v_mfma_f32_16x16x32_bf16 v[106:109], v[204:207], v[224:227], v[106:109]
	v_mfma_f32_16x16x32_bf16 v[98:101], v[212:215], v[224:227], v[98:101]
	v_mfma_f32_16x16x32_bf16 v[90:93], v[204:207], v[228:231], v[90:93]
	v_mfma_f32_16x16x32_bf16 v[82:85], v[212:215], v[228:231], v[82:85]
	v_mfma_f32_16x16x32_bf16 v[78:81], v[204:207], v[240:243], v[78:81]
	v_mfma_f32_16x16x32_bf16 v[74:77], v[212:215], v[240:243], v[74:77]
	v_mfma_f32_16x16x32_bf16 v[70:73], v[204:207], v[244:247], v[70:73]
	v_mfma_f32_16x16x32_bf16 v[66:69], v[212:215], v[244:247], v[66:69]
	s_setprio 0
	s_barrier
	s_add_i32 s34, s65, s33
	v_lshl_add_u64 v[240:241], v[248:249], 0, s[8:9]
	s_mov_b32 m0, s34
	ds_read_b128 v[160:163], v177 offset:49152
	ds_read_b128 v[164:167], v177 offset:51200
	ds_read_b128 v[216:219], v178 offset:49152
	ds_read_b128 v[220:223], v178 offset:51200
	ds_read_b128 v[224:227], v177 offset:53248
	ds_read_b128 v[228:231], v177 offset:55296
	ds_read_b128 v[232:235], v178 offset:53248
	ds_read_b128 v[236:239], v178 offset:55296
	global_load_lds_dwordx4 v[240:241], off
	s_add_i32 m0, s34, 0x2000
	s_add_u32 s30, s30, 0x80080
	v_lshl_add_u64 v[240:241], v[250:251], 0, s[8:9]
	s_addc_u32 s31, s31, 0
	s_add_i32 s34, s67, s33
	global_load_lds_dwordx4 v[240:241], off
	s_mov_b32 m0, s34
	s_nop 0
	global_load_lds_dwordx4 v146, s[30:31]
	s_add_i32 m0, s34, 0x2000
	s_nop 0
	global_load_lds_dwordx4 v148, s[30:31]
	s_waitcnt vmcnt(6)
	s_waitcnt lgkmcnt(0)
	s_barrier
	s_setprio 1
	s_waitcnt lgkmcnt(0)
	v_mfma_f32_16x16x32_bf16 v[62:65], v[184:187], v[160:163], v[62:65]
	v_mfma_f32_16x16x32_bf16 v[58:61], v[192:195], v[160:163], v[58:61]
	v_mfma_f32_16x16x32_bf16 v[50:53], v[184:187], v[164:167], v[50:53]
	v_mfma_f32_16x16x32_bf16 v[42:45], v[192:195], v[164:167], v[42:45]
	v_mfma_f32_16x16x32_bf16 v[34:37], v[184:187], v[224:227], v[34:37]
	v_mfma_f32_16x16x32_bf16 v[26:29], v[192:195], v[224:227], v[26:29]
	v_mfma_f32_16x16x32_bf16 v[18:21], v[184:187], v[228:231], v[18:21]
	v_mfma_f32_16x16x32_bf16 v[10:13], v[192:195], v[228:231], v[10:13]
	v_mfma_f32_16x16x32_bf16 v[62:65], v[188:191], v[216:219], v[62:65]
	v_mfma_f32_16x16x32_bf16 v[58:61], v[196:199], v[216:219], v[58:61]
	v_mfma_f32_16x16x32_bf16 v[50:53], v[188:191], v[220:223], v[50:53]
	v_mfma_f32_16x16x32_bf16 v[42:45], v[196:199], v[220:223], v[42:45]
	v_mfma_f32_16x16x32_bf16 v[34:37], v[188:191], v[232:235], v[34:37]
	v_mfma_f32_16x16x32_bf16 v[26:29], v[196:199], v[232:235], v[26:29]
	v_mfma_f32_16x16x32_bf16 v[18:21], v[188:191], v[236:239], v[18:21]
	v_mfma_f32_16x16x32_bf16 v[10:13], v[196:199], v[236:239], v[10:13]
	s_setprio 0
	s_setprio 1
	v_mfma_f32_16x16x32_bf16 v[54:57], v[200:203], v[160:163], v[54:57]
	v_mfma_f32_16x16x32_bf16 v[46:49], v[208:211], v[160:163], v[46:49]
	v_mfma_f32_16x16x32_bf16 v[38:41], v[200:203], v[164:167], v[38:41]
	v_mfma_f32_16x16x32_bf16 v[30:33], v[208:211], v[164:167], v[30:33]
	v_mfma_f32_16x16x32_bf16 v[22:25], v[200:203], v[224:227], v[22:25]
	v_mfma_f32_16x16x32_bf16 v[14:17], v[208:211], v[224:227], v[14:17]
	v_mfma_f32_16x16x32_bf16 v[6:9], v[200:203], v[228:231], v[6:9]
	v_mfma_f32_16x16x32_bf16 v[2:5], v[208:211], v[228:231], v[2:5]
	v_mfma_f32_16x16x32_bf16 v[54:57], v[204:207], v[216:219], v[54:57]
	v_mfma_f32_16x16x32_bf16 v[46:49], v[212:215], v[216:219], v[46:49]
	v_mfma_f32_16x16x32_bf16 v[38:41], v[204:207], v[220:223], v[38:41]
	v_mfma_f32_16x16x32_bf16 v[30:33], v[212:215], v[220:223], v[30:33]
	v_mfma_f32_16x16x32_bf16 v[22:25], v[204:207], v[232:235], v[22:25]
	v_mfma_f32_16x16x32_bf16 v[14:17], v[212:215], v[232:235], v[14:17]
	v_mfma_f32_16x16x32_bf16 v[6:9], v[204:207], v[236:239], v[6:9]
	v_mfma_f32_16x16x32_bf16 v[2:5], v[212:215], v[236:239], v[2:5]
	s_setprio 0
	s_barrier
	s_add_i32 s76, s76, 2
	s_add_u32 s28, s28, 0x100
	s_addc_u32 s29, s29, 0
	s_cmp_gt_u32 s76, 29
	s_cbranch_scc1 .LBB0_389

.Lp6_first:
	ds_read_b128 v[18:21], v208
	ds_read_b128 v[22:25], v209
	ds_read_b128 v[26:29], v208 offset:2048
	ds_read_b128 v[30:33], v209 offset:2048
	ds_read_b128 v[2:5], v208 offset:16384
	ds_read_b128 v[6:9], v209 offset:16384
	ds_read_b128 v[10:13], v208 offset:18432
	ds_read_b128 v[14:17], v209 offset:18432
	v_lshl_add_u64 v[200:201], v[190:191], 0, s[40:41]
	s_add_i32 m0, s35, 0x8000
	ds_read_b128 v[218:221], v211
	ds_read_b128 v[226:229], v211 offset:2048
	ds_read_b128 v[222:225], v212
	ds_read_b128 v[230:233], v212 offset:2048
	ds_read_b128 v[234:237], v211 offset:4096
	ds_read_b128 v[242:245], v211 offset:6144
	ds_read_b128 v[238:241], v212 offset:4096
	ds_read_b128 v[246:249], v212 offset:6144
	global_load_lds_dwordx4 v[200:201], off
	v_lshl_add_u64 v[200:201], v[188:189], 0, s[40:41]
	s_add_i32 m0, s35, 0xa000
	s_nop 0
	global_load_lds_dwordx4 v[200:201], off
	v_lshl_add_u64 v[200:201], v[186:187], 0, s[40:41]
	s_add_i32 m0, s35, 0xc000
	s_nop 0
	global_load_lds_dwordx4 v[200:201], off
	v_lshl_add_u64 v[200:201], v[184:185], 0, s[40:41]
	s_add_i32 m0, s35, 0xe000
	s_nop 0
	global_load_lds_dwordx4 v[200:201], off
	s_waitcnt vmcnt(8)
	s_waitcnt lgkmcnt(0)
	s_barrier
	s_setprio 1
	s_waitcnt lgkmcnt(0)
	v_mfma_f32_16x16x128_f8f6f4 v[158:161], v[18:25], v[218:225], 0
	s_add_u32 s44, s2, s40
	s_addc_u32 s45, s3, s41
	s_add_u32 s84, s44, 0x56800100
	s_addc_u32 s85, s45, 0
	v_mfma_f32_16x16x128_f8f6f4 v[154:157], v[26:33], v[218:225], 0
	s_and_b64 s[44:45], s[42:43], exec
	s_cselect_b32 s45, s9, s85
	s_cselect_b32 s44, s8, s84
	s_add_u32 s84, s29, s40
	v_mfma_f32_16x16x128_f8f6f4 v[150:153], v[18:25], v[226:233], 0
	s_addc_u32 s85, s37, s41
	s_and_b64 s[42:43], s[42:43], exec
	s_cselect_b32 s43, s31, s85
	s_cselect_b32 s42, s30, s84
	v_mfma_f32_16x16x128_f8f6f4 v[146:149], v[26:33], v[226:233], 0
	v_mfma_f32_16x16x128_f8f6f4 v[126:129], v[18:25], v[234:241], 0
	v_mfma_f32_16x16x128_f8f6f4 v[122:125], v[26:33], v[234:241], 0
	v_mfma_f32_16x16x128_f8f6f4 v[110:113], v[18:25], v[242:249], 0
	v_mfma_f32_16x16x128_f8f6f4 v[106:109], v[26:33], v[242:249], 0
	s_setprio 0
	s_setprio 1
	v_mfma_f32_16x16x128_f8f6f4 v[142:145], v[2:9], v[218:225], 0
	v_mfma_f32_16x16x128_f8f6f4 v[138:141], v[10:17], v[218:225], 0
	v_mfma_f32_16x16x128_f8f6f4 v[134:137], v[2:9], v[226:233], 0
	v_mfma_f32_16x16x128_f8f6f4 v[130:133], v[10:17], v[226:233], 0
	v_mfma_f32_16x16x128_f8f6f4 v[118:121], v[2:9], v[234:241], 0
	v_mfma_f32_16x16x128_f8f6f4 v[114:117], v[10:17], v[234:241], 0
	v_mfma_f32_16x16x128_f8f6f4 v[102:105], v[2:9], v[242:249], 0
	v_mfma_f32_16x16x128_f8f6f4 v[98:101], v[10:17], v[242:249], 0
	s_setprio 0
	s_barrier
	s_add_i32 s84, s68, s33
	v_lshl_add_u64 v[200:201], s[42:43], 0, v[164:165]
	s_mov_b32 m0, s84
	ds_read_b128 v[218:221], v211 offset:16384
	ds_read_b128 v[226:229], v211 offset:18432
	ds_read_b128 v[222:225], v212 offset:16384
	ds_read_b128 v[230:233], v212 offset:18432
	ds_read_b128 v[234:237], v211 offset:20480
	ds_read_b128 v[242:245], v211 offset:22528
	ds_read_b128 v[238:241], v212 offset:20480
	ds_read_b128 v[246:249], v212 offset:22528
	global_load_lds_dwordx4 v[200:201], off
	s_add_i32 m0, s84, 0x2000
	s_add_u32 s84, s42, 0x40000
	v_lshl_add_u64 v[202:203], s[42:43], 0, v[166:167]
	s_addc_u32 s85, s43, 0
	s_add_i32 s86, s70, s33
	global_load_lds_dwordx4 v[202:203], off
	s_mov_b32 m0, s86
	s_nop 0
	global_load_lds_dwordx4 v164, s[84:85]
	s_add_i32 m0, s86, 0x2000
	s_nop 0
	global_load_lds_dwordx4 v166, s[84:85]
	s_waitcnt vmcnt(6)
	s_waitcnt lgkmcnt(0)
	s_barrier
	s_setprio 1
	s_waitcnt lgkmcnt(0)
	v_mfma_f32_16x16x128_f8f6f4 v[94:97], v[18:25], v[218:225], 0
	v_mfma_f32_16x16x128_f8f6f4 v[90:93], v[26:33], v[218:225], 0
	v_mfma_f32_16x16x128_f8f6f4 v[78:81], v[18:25], v[226:233], 0
	v_mfma_f32_16x16x128_f8f6f4 v[74:77], v[26:33], v[226:233], 0
	v_mfma_f32_16x16x128_f8f6f4 v[62:65], v[18:25], v[234:241], 0
	v_mfma_f32_16x16x128_f8f6f4 v[58:61], v[26:33], v[234:241], 0
	v_mfma_f32_16x16x128_f8f6f4 v[46:49], v[18:25], v[242:249], 0
	v_mfma_f32_16x16x128_f8f6f4 v[42:45], v[26:33], v[242:249], 0
	s_setprio 0
	s_setprio 1
	v_mfma_f32_16x16x128_f8f6f4 v[86:89], v[2:9], v[218:225], 0
	v_mfma_f32_16x16x128_f8f6f4 v[82:85], v[10:17], v[218:225], 0
	v_mfma_f32_16x16x128_f8f6f4 v[70:73], v[2:9], v[226:233], 0
	v_mfma_f32_16x16x128_f8f6f4 v[66:69], v[10:17], v[226:233], 0
	v_mfma_f32_16x16x128_f8f6f4 v[54:57], v[2:9], v[234:241], 0
	v_mfma_f32_16x16x128_f8f6f4 v[50:53], v[10:17], v[234:241], 0
	v_mfma_f32_16x16x128_f8f6f4 v[38:41], v[2:9], v[242:249], 0
	v_mfma_f32_16x16x128_f8f6f4 v[34:37], v[10:17], v[242:249], 0
	s_setprio 0
	s_barrier
	s_branch .Lp6_blk3

.LBB0_777:
	s_cmp_eq_u32 s40, 0
	s_cbranch_scc1 .Lp6_first
	ds_read_b128 v[18:21], v208
	ds_read_b128 v[22:25], v209
	ds_read_b128 v[26:29], v208 offset:2048
	ds_read_b128 v[30:33], v209 offset:2048
	ds_read_b128 v[2:5], v208 offset:16384
	ds_read_b128 v[6:9], v209 offset:16384
	ds_read_b128 v[10:13], v208 offset:18432
	ds_read_b128 v[14:17], v209 offset:18432
	v_lshl_add_u64 v[200:201], v[190:191], 0, s[40:41]
	s_add_i32 m0, s35, 0x8000
	ds_read_b128 v[218:221], v211
	ds_read_b128 v[226:229], v211 offset:2048
	ds_read_b128 v[222:225], v212
	ds_read_b128 v[230:233], v212 offset:2048
	ds_read_b128 v[234:237], v211 offset:4096
	ds_read_b128 v[242:245], v211 offset:6144
	ds_read_b128 v[238:241], v212 offset:4096
	ds_read_b128 v[246:249], v212 offset:6144
	global_load_lds_dwordx4 v[200:201], off
	v_lshl_add_u64 v[200:201], v[188:189], 0, s[40:41]
	s_add_i32 m0, s35, 0xa000
	s_nop 0
	global_load_lds_dwordx4 v[200:201], off
	v_lshl_add_u64 v[200:201], v[186:187], 0, s[40:41]
	s_add_i32 m0, s35, 0xc000
	s_nop 0
	global_load_lds_dwordx4 v[200:201], off
	v_lshl_add_u64 v[200:201], v[184:185], 0, s[40:41]
	s_add_i32 m0, s35, 0xe000
	s_nop 0
	global_load_lds_dwordx4 v[200:201], off
	s_waitcnt vmcnt(8)
	s_waitcnt lgkmcnt(0)
	s_barrier
	s_setprio 1
	s_waitcnt lgkmcnt(0)
	v_mfma_f32_16x16x128_f8f6f4 v[158:161], v[18:25], v[218:225], v[158:161]
	s_add_u32 s44, s2, s40
	s_addc_u32 s45, s3, s41
	s_add_u32 s84, s44, 0x56800100
	s_addc_u32 s85, s45, 0
	v_mfma_f32_16x16x128_f8f6f4 v[154:157], v[26:33], v[218:225], v[154:157]
	s_and_b64 s[44:45], s[42:43], exec
	s_cselect_b32 s45, s9, s85
	s_cselect_b32 s44, s8, s84
	s_add_u32 s84, s29, s40
	v_mfma_f32_16x16x128_f8f6f4 v[150:153], v[18:25], v[226:233], v[150:153]
	s_addc_u32 s85, s37, s41
	s_and_b64 s[42:43], s[42:43], exec
	s_cselect_b32 s43, s31, s85
	s_cselect_b32 s42, s30, s84
	v_mfma_f32_16x16x128_f8f6f4 v[146:149], v[26:33], v[226:233], v[146:149]
	v_mfma_f32_16x16x128_f8f6f4 v[126:129], v[18:25], v[234:241], v[126:129]
	v_mfma_f32_16x16x128_f8f6f4 v[122:125], v[26:33], v[234:241], v[122:125]
	v_mfma_f32_16x16x128_f8f6f4 v[110:113], v[18:25], v[242:249], v[110:113]
	v_mfma_f32_16x16x128_f8f6f4 v[106:109], v[26:33], v[242:249], v[106:109]
	s_setprio 0
	s_setprio 1
	v_mfma_f32_16x16x128_f8f6f4 v[142:145], v[2:9], v[218:225], v[142:145]
	v_mfma_f32_16x16x128_f8f6f4 v[138:141], v[10:17], v[218:225], v[138:141]
	v_mfma_f32_16x16x128_f8f6f4 v[134:137], v[2:9], v[226:233], v[134:137]
	v_mfma_f32_16x16x128_f8f6f4 v[130:133], v[10:17], v[226:233], v[130:133]
	v_mfma_f32_16x16x128_f8f6f4 v[118:121], v[2:9], v[234:241], v[118:121]
	v_mfma_f32_16x16x128_f8f6f4 v[114:117], v[10:17], v[234:241], v[114:117]
	v_mfma_f32_16x16x128_f8f6f4 v[102:105], v[2:9], v[242:249], v[102:105]
	v_mfma_f32_16x16x128_f8f6f4 v[98:101], v[10:17], v[242:249], v[98:101]
	s_setprio 0
	s_barrier
	s_add_i32 s84, s68, s33
	v_lshl_add_u64 v[200:201], s[42:43], 0, v[164:165]
	s_mov_b32 m0, s84
	ds_read_b128 v[218:221], v211 offset:16384
	ds_read_b128 v[226:229], v211 offset:18432
	ds_read_b128 v[222:225], v212 offset:16384
	ds_read_b128 v[230:233], v212 offset:18432
	ds_read_b128 v[234:237], v211 offset:20480
	ds_read_b128 v[242:245], v211 offset:22528
	ds_read_b128 v[238:241], v212 offset:20480
	ds_read_b128 v[246:249], v212 offset:22528
	global_load_lds_dwordx4 v[200:201], off
	s_add_i32 m0, s84, 0x2000
	s_add_u32 s84, s42, 0x40000
	v_lshl_add_u64 v[202:203], s[42:43], 0, v[166:167]
	s_addc_u32 s85, s43, 0
	s_add_i32 s86, s70, s33
	global_load_lds_dwordx4 v[202:203], off
	s_mov_b32 m0, s86
	s_nop 0
	global_load_lds_dwordx4 v164, s[84:85]
	s_add_i32 m0, s86, 0x2000
	s_nop 0
	global_load_lds_dwordx4 v166, s[84:85]
	s_waitcnt vmcnt(6)
	s_waitcnt lgkmcnt(0)
	s_barrier
	s_setprio 1
	s_waitcnt lgkmcnt(0)
	v_mfma_f32_16x16x128_f8f6f4 v[94:97], v[18:25], v[218:225], v[94:97]
	v_mfma_f32_16x16x128_f8f6f4 v[90:93], v[26:33], v[218:225], v[90:93]
	v_mfma_f32_16x16x128_f8f6f4 v[78:81], v[18:25], v[226:233], v[78:81]
	v_mfma_f32_16x16x128_f8f6f4 v[74:77], v[26:33], v[226:233], v[74:77]
	v_mfma_f32_16x16x128_f8f6f4 v[62:65], v[18:25], v[234:241], v[62:65]
	v_mfma_f32_16x16x128_f8f6f4 v[58:61], v[26:33], v[234:241], v[58:61]
	v_mfma_f32_16x16x128_f8f6f4 v[46:49], v[18:25], v[242:249], v[46:49]
	v_mfma_f32_16x16x128_f8f6f4 v[42:45], v[26:33], v[242:249], v[42:45]
	s_setprio 0
	s_setprio 1
	v_mfma_f32_16x16x128_f8f6f4 v[86:89], v[2:9], v[218:225], v[86:89]
	v_mfma_f32_16x16x128_f8f6f4 v[82:85], v[10:17], v[218:225], v[82:85]
	v_mfma_f32_16x16x128_f8f6f4 v[70:73], v[2:9], v[226:233], v[70:73]
	v_mfma_f32_16x16x128_f8f6f4 v[66:69], v[10:17], v[226:233], v[66:69]
	v_mfma_f32_16x16x128_f8f6f4 v[54:57], v[2:9], v[234:241], v[54:57]
	v_mfma_f32_16x16x128_f8f6f4 v[50:53], v[10:17], v[234:241], v[50:53]
	v_mfma_f32_16x16x128_f8f6f4 v[38:41], v[2:9], v[242:249], v[38:41]
	v_mfma_f32_16x16x128_f8f6f4 v[34:37], v[10:17], v[242:249], v[34:37]
	s_setprio 0
	s_barrier
.Lp6_blk3:
	ds_read_b128 v[2:5], v208 offset:32768
	ds_read_b128 v[6:9], v209 offset:32768
	ds_read_b128 v[10:13], v208 offset:34816
	ds_read_b128 v[14:17], v209 offset:34816
	ds_read_b128 v[18:21], v208 offset:49152
	ds_read_b128 v[22:25], v209 offset:49152
	ds_read_b128 v[26:29], v208 offset:51200
	ds_read_b128 v[30:33], v209 offset:51200
	s_mov_b32 m0, s35
	ds_read_b128 v[218:221], v211 offset:32768
	ds_read_b128 v[226:229], v211 offset:34816
	ds_read_b128 v[222:225], v212 offset:32768
	ds_read_b128 v[230:233], v212 offset:34816
	ds_read_b128 v[234:237], v211 offset:36864
	ds_read_b128 v[242:245], v211 offset:38912
	ds_read_b128 v[238:241], v212 offset:36864
	ds_read_b128 v[246:249], v212 offset:38912
	global_load_lds_dwordx4 v198, s[44:45]
	s_mov_b32 m0, s55
	global_load_lds_dwordx4 v196, s[44:45]
	s_mov_b32 m0, s64
	global_load_lds_dwordx4 v194, s[44:45]
	s_mov_b32 m0, s65
	s_nop 0
	global_load_lds_dwordx4 v192, s[44:45]
	s_waitcnt vmcnt(8)
	s_waitcnt lgkmcnt(0)
	s_barrier
	s_setprio 1
	s_waitcnt lgkmcnt(0)
	v_mfma_f32_16x16x128_f8f6f4 v[158:161], v[2:9], v[218:225], v[158:161]
	v_mfma_f32_16x16x128_f8f6f4 v[154:157], v[10:17], v[218:225], v[154:157]
	v_mfma_f32_16x16x128_f8f6f4 v[150:153], v[2:9], v[226:233], v[150:153]
	v_mfma_f32_16x16x128_f8f6f4 v[146:149], v[10:17], v[226:233], v[146:149]
	v_mfma_f32_16x16x128_f8f6f4 v[126:129], v[2:9], v[234:241], v[126:129]
	v_mfma_f32_16x16x128_f8f6f4 v[122:125], v[10:17], v[234:241], v[122:125]
	v_mfma_f32_16x16x128_f8f6f4 v[110:113], v[2:9], v[242:249], v[110:113]
	v_mfma_f32_16x16x128_f8f6f4 v[106:109], v[10:17], v[242:249], v[106:109]
	s_setprio 0
	s_setprio 1
	v_mfma_f32_16x16x128_f8f6f4 v[142:145], v[18:25], v[218:225], v[142:145]
	v_mfma_f32_16x16x128_f8f6f4 v[138:141], v[26:33], v[218:225], v[138:141]
	v_mfma_f32_16x16x128_f8f6f4 v[134:137], v[18:25], v[226:233], v[134:137]
	v_mfma_f32_16x16x128_f8f6f4 v[130:133], v[26:33], v[226:233], v[130:133]
	v_mfma_f32_16x16x128_f8f6f4 v[118:121], v[18:25], v[234:241], v[118:121]
	v_mfma_f32_16x16x128_f8f6f4 v[114:117], v[26:33], v[234:241], v[114:117]
	v_mfma_f32_16x16x128_f8f6f4 v[102:105], v[18:25], v[242:249], v[102:105]
	v_mfma_f32_16x16x128_f8f6f4 v[98:101], v[26:33], v[242:249], v[98:101]
	s_setprio 0
	s_barrier
	s_add_i32 s44, s72, s33
	v_lshl_add_u64 v[200:201], v[200:201], 0, s[10:11]
	s_mov_b32 m0, s44
	ds_read_b128 v[192:195], v211 offset:49152
	ds_read_b128 v[218:221], v211 offset:51200
	ds_read_b128 v[196:199], v212 offset:49152
	ds_read_b128 v[222:225], v212 offset:51200
	ds_read_b128 v[226:229], v211 offset:53248
	ds_read_b128 v[234:237], v211 offset:55296
	ds_read_b128 v[230:233], v212 offset:53248
	ds_read_b128 v[238:241], v212 offset:55296
	global_load_lds_dwordx4 v[200:201], off
	s_add_i32 m0, s44, 0x2000
	s_add_u32 s42, s42, 0x40080
	v_lshl_add_u64 v[200:201], v[202:203], 0, s[10:11]
	s_addc_u32 s43, s43, 0
	s_add_i32 s44, s74, s33
	global_load_lds_dwordx4 v[200:201], off
	s_mov_b32 m0, s44
	s_nop 0
	global_load_lds_dwordx4 v164, s[42:43]
	s_add_i32 m0, s44, 0x2000
	s_nop 0
	global_load_lds_dwordx4 v166, s[42:43]
	s_waitcnt vmcnt(6)
	s_waitcnt lgkmcnt(0)
	s_barrier
	s_setprio 1
	s_waitcnt lgkmcnt(0)
	v_mfma_f32_16x16x128_f8f6f4 v[94:97], v[2:9], v[192:199], v[94:97]
	v_mfma_f32_16x16x128_f8f6f4 v[90:93], v[10:17], v[192:199], v[90:93]
	v_mfma_f32_16x16x128_f8f6f4 v[78:81], v[2:9], v[218:225], v[78:81]
	v_mfma_f32_16x16x128_f8f6f4 v[74:77], v[10:17], v[218:225], v[74:77]
	v_mfma_f32_16x16x128_f8f6f4 v[62:65], v[2:9], v[226:233], v[62:65]
	v_mfma_f32_16x16x128_f8f6f4 v[58:61], v[10:17], v[226:233], v[58:61]
	v_mfma_f32_16x16x128_f8f6f4 v[46:49], v[2:9], v[234:241], v[46:49]
	v_mfma_f32_16x16x128_f8f6f4 v[42:45], v[10:17], v[234:241], v[42:45]
	s_setprio 0
	s_setprio 1
	v_mfma_f32_16x16x128_f8f6f4 v[86:89], v[18:25], v[192:199], v[86:89]
	v_mfma_f32_16x16x128_f8f6f4 v[82:85], v[26:33], v[192:199], v[82:85]
	v_mfma_f32_16x16x128_f8f6f4 v[70:73], v[18:25], v[218:225], v[70:73]
	v_mfma_f32_16x16x128_f8f6f4 v[66:69], v[26:33], v[218:225], v[66:69]
	v_mfma_f32_16x16x128_f8f6f4 v[54:57], v[18:25], v[226:233], v[54:57]
	v_mfma_f32_16x16x128_f8f6f4 v[50:53], v[26:33], v[226:233], v[50:53]
	v_mfma_f32_16x16x128_f8f6f4 v[38:41], v[18:25], v[234:241], v[38:41]
	v_mfma_f32_16x16x128_f8f6f4 v[34:37], v[26:33], v[234:241], v[34:37]
	s_setprio 0
	s_barrier
	s_add_i32 s83, s83, 2
	s_add_u32 s40, s40, 0x100
	s_addc_u32 s41, s41, 0
	s_cmp_gt_u32 s83, 13
	s_cbranch_scc1 .LBB0_781

.Lp7_first:
	ds_read_b128 v[18:21], v210
	ds_read_b128 v[22:25], v211
	ds_read_b128 v[26:29], v210 offset:2048
	ds_read_b128 v[30:33], v211 offset:2048
	ds_read_b128 v[2:5], v210 offset:16384
	ds_read_b128 v[6:9], v211 offset:16384
	ds_read_b128 v[10:13], v210 offset:18432
	ds_read_b128 v[14:17], v211 offset:18432
	v_lshl_add_u64 v[200:201], v[190:191], 0, s[44:45]
	s_add_i32 m0, s41, 0x8000
	ds_read_b128 v[220:223], v213
	ds_read_b128 v[228:231], v213 offset:2048
	ds_read_b128 v[224:227], v214
	ds_read_b128 v[232:235], v214 offset:2048
	ds_read_b128 v[236:239], v213 offset:4096
	ds_read_b128 v[244:247], v213 offset:6144
	ds_read_b128 v[240:243], v214 offset:4096
	ds_read_b128 v[248:251], v214 offset:6144
	global_load_lds_dwordx4 v[200:201], off
	v_lshl_add_u64 v[200:201], v[188:189], 0, s[44:45]
	s_add_i32 m0, s41, 0xa000
	s_nop 0
	global_load_lds_dwordx4 v[200:201], off
	v_lshl_add_u64 v[200:201], v[186:187], 0, s[44:45]
	s_add_i32 m0, s41, 0xc000
	s_nop 0
	global_load_lds_dwordx4 v[200:201], off
	v_lshl_add_u64 v[200:201], v[184:185], 0, s[44:45]
	s_add_i32 m0, s41, 0xe000
	s_nop 0
	global_load_lds_dwordx4 v[200:201], off
	s_waitcnt vmcnt(8)
	s_waitcnt lgkmcnt(0)
	s_barrier
	s_setprio 1
	s_waitcnt lgkmcnt(0)
	v_mfma_f32_16x16x128_f8f6f4 v[158:161], v[18:25], v[220:227], 0
	s_add_u32 s48, s2, s44
	s_addc_u32 s49, s3, s45
	s_add_u32 s81, s48, 0x3e800100
	s_addc_u32 s82, s49, 0
	v_mfma_f32_16x16x128_f8f6f4 v[154:157], v[26:33], v[220:227], 0
	s_and_b64 s[48:49], s[46:47], exec
	s_cselect_b32 s49, s9, s82
	s_cselect_b32 s48, s8, s81
	s_add_u32 s81, s35, s44
	v_mfma_f32_16x16x128_f8f6f4 v[150:153], v[18:25], v[228:235], 0
	s_addc_u32 s82, s37, s45
	s_and_b64 s[46:47], s[46:47], exec
	s_cselect_b32 s47, s39, s82
	s_cselect_b32 s46, s38, s81
	v_mfma_f32_16x16x128_f8f6f4 v[146:149], v[26:33], v[228:235], 0
	v_mfma_f32_16x16x128_f8f6f4 v[142:145], v[18:25], v[236:243], 0
	v_mfma_f32_16x16x128_f8f6f4 v[138:141], v[26:33], v[236:243], 0
	v_mfma_f32_16x16x128_f8f6f4 v[134:137], v[18:25], v[244:251], 0
	v_mfma_f32_16x16x128_f8f6f4 v[130:133], v[26:33], v[244:251], 0
	s_setprio 0
	s_setprio 1
	v_mfma_f32_16x16x128_f8f6f4 v[102:105], v[2:9], v[220:227], 0
	v_mfma_f32_16x16x128_f8f6f4 v[94:97], v[10:17], v[220:227], 0
	v_mfma_f32_16x16x128_f8f6f4 v[86:89], v[2:9], v[228:235], 0
	v_mfma_f32_16x16x128_f8f6f4 v[82:85], v[10:17], v[228:235], 0
	v_mfma_f32_16x16x128_f8f6f4 v[78:81], v[2:9], v[236:243], 0
	v_mfma_f32_16x16x128_f8f6f4 v[74:77], v[10:17], v[236:243], 0
	v_mfma_f32_16x16x128_f8f6f4 v[70:73], v[2:9], v[244:251], 0
	v_mfma_f32_16x16x128_f8f6f4 v[66:69], v[10:17], v[244:251], 0
	s_setprio 0
	s_barrier
	s_add_i32 s81, s66, s51
	v_lshl_add_u64 v[200:201], s[46:47], 0, v[162:163]
	s_mov_b32 m0, s81
	ds_read_b128 v[220:223], v213 offset:16384
	ds_read_b128 v[228:231], v213 offset:18432
	ds_read_b128 v[224:227], v214 offset:16384
	ds_read_b128 v[232:235], v214 offset:18432
	ds_read_b128 v[236:239], v213 offset:20480
	ds_read_b128 v[244:247], v213 offset:22528
	ds_read_b128 v[240:243], v214 offset:20480
	ds_read_b128 v[248:251], v214 offset:22528
	global_load_lds_dwordx4 v[200:201], off
	s_add_i32 m0, s81, 0x2000
	s_add_u32 s82, s46, 0x40000
	v_lshl_add_u64 v[202:203], s[46:47], 0, v[164:165]
	s_addc_u32 s83, s47, 0
	s_add_i32 s81, s68, s51
	global_load_lds_dwordx4 v[202:203], off
	s_mov_b32 m0, s81
	s_nop 0
	global_load_lds_dwordx4 v162, s[82:83]
	s_add_i32 m0, s81, 0x2000
	s_nop 0
	global_load_lds_dwordx4 v164, s[82:83]
	s_waitcnt vmcnt(6)
	s_waitcnt lgkmcnt(0)
	s_barrier
	s_setprio 1
	s_waitcnt lgkmcnt(0)
	v_mfma_f32_16x16x128_f8f6f4 v[126:129], v[18:25], v[220:227], 0
	v_mfma_f32_16x16x128_f8f6f4 v[122:125], v[26:33], v[220:227], 0
	v_mfma_f32_16x16x128_f8f6f4 v[118:121], v[18:25], v[228:235], 0
	v_mfma_f32_16x16x128_f8f6f4 v[114:117], v[26:33], v[228:235], 0
	v_mfma_f32_16x16x128_f8f6f4 v[110:113], v[18:25], v[236:243], 0
	v_mfma_f32_16x16x128_f8f6f4 v[106:109], v[26:33], v[236:243], 0
	v_mfma_f32_16x16x128_f8f6f4 v[98:101], v[18:25], v[244:251], 0
	v_mfma_f32_16x16x128_f8f6f4 v[90:93], v[26:33], v[244:251], 0
	s_setprio 0
	s_setprio 1
	v_mfma_f32_16x16x128_f8f6f4 v[62:65], v[2:9], v[220:227], 0
	v_mfma_f32_16x16x128_f8f6f4 v[58:61], v[10:17], v[220:227], 0
	v_mfma_f32_16x16x128_f8f6f4 v[54:57], v[2:9], v[228:235], 0
	v_mfma_f32_16x16x128_f8f6f4 v[50:53], v[10:17], v[228:235], 0
	v_mfma_f32_16x16x128_f8f6f4 v[46:49], v[2:9], v[236:243], 0
	v_mfma_f32_16x16x128_f8f6f4 v[42:45], v[10:17], v[236:243], 0
	v_mfma_f32_16x16x128_f8f6f4 v[38:41], v[2:9], v[244:251], 0
	v_mfma_f32_16x16x128_f8f6f4 v[34:37], v[10:17], v[244:251], 0
	s_setprio 0
	s_barrier
	s_branch .Lp7_blk3

.LBB0_862:
	s_cmp_eq_u32 s44, 0
	s_cbranch_scc1 .Lp7_first
	ds_read_b128 v[18:21], v210
	ds_read_b128 v[22:25], v211
	ds_read_b128 v[26:29], v210 offset:2048
	ds_read_b128 v[30:33], v211 offset:2048
	ds_read_b128 v[2:5], v210 offset:16384
	ds_read_b128 v[6:9], v211 offset:16384
	ds_read_b128 v[10:13], v210 offset:18432
	ds_read_b128 v[14:17], v211 offset:18432
	v_lshl_add_u64 v[200:201], v[190:191], 0, s[44:45]
	s_add_i32 m0, s41, 0x8000
	ds_read_b128 v[220:223], v213
	ds_read_b128 v[228:231], v213 offset:2048
	ds_read_b128 v[224:227], v214
	ds_read_b128 v[232:235], v214 offset:2048
	ds_read_b128 v[236:239], v213 offset:4096
	ds_read_b128 v[244:247], v213 offset:6144
	ds_read_b128 v[240:243], v214 offset:4096
	ds_read_b128 v[248:251], v214 offset:6144
	global_load_lds_dwordx4 v[200:201], off
	v_lshl_add_u64 v[200:201], v[188:189], 0, s[44:45]
	s_add_i32 m0, s41, 0xa000
	s_nop 0
	global_load_lds_dwordx4 v[200:201], off
	v_lshl_add_u64 v[200:201], v[186:187], 0, s[44:45]
	s_add_i32 m0, s41, 0xc000
	s_nop 0
	global_load_lds_dwordx4 v[200:201], off
	v_lshl_add_u64 v[200:201], v[184:185], 0, s[44:45]
	s_add_i32 m0, s41, 0xe000
	s_nop 0
	global_load_lds_dwordx4 v[200:201], off
	s_waitcnt vmcnt(8)
	s_waitcnt lgkmcnt(0)
	s_barrier
	s_setprio 1
	s_waitcnt lgkmcnt(0)
	v_mfma_f32_16x16x128_f8f6f4 v[158:161], v[18:25], v[220:227], v[158:161]
	s_add_u32 s48, s2, s44
	s_addc_u32 s49, s3, s45
	s_add_u32 s81, s48, 0x3e800100
	s_addc_u32 s82, s49, 0
	v_mfma_f32_16x16x128_f8f6f4 v[154:157], v[26:33], v[220:227], v[154:157]
	s_and_b64 s[48:49], s[46:47], exec
	s_cselect_b32 s49, s9, s82
	s_cselect_b32 s48, s8, s81
	s_add_u32 s81, s35, s44
	v_mfma_f32_16x16x128_f8f6f4 v[150:153], v[18:25], v[228:235], v[150:153]
	s_addc_u32 s82, s37, s45
	s_and_b64 s[46:47], s[46:47], exec
	s_cselect_b32 s47, s39, s82
	s_cselect_b32 s46, s38, s81
	v_mfma_f32_16x16x128_f8f6f4 v[146:149], v[26:33], v[228:235], v[146:149]
	v_mfma_f32_16x16x128_f8f6f4 v[142:145], v[18:25], v[236:243], v[142:145]
	v_mfma_f32_16x16x128_f8f6f4 v[138:141], v[26:33], v[236:243], v[138:141]
	v_mfma_f32_16x16x128_f8f6f4 v[134:137], v[18:25], v[244:251], v[134:137]
	v_mfma_f32_16x16x128_f8f6f4 v[130:133], v[26:33], v[244:251], v[130:133]
	s_setprio 0
	s_setprio 1
	v_mfma_f32_16x16x128_f8f6f4 v[102:105], v[2:9], v[220:227], v[102:105]
	v_mfma_f32_16x16x128_f8f6f4 v[94:97], v[10:17], v[220:227], v[94:97]
	v_mfma_f32_16x16x128_f8f6f4 v[86:89], v[2:9], v[228:235], v[86:89]
	v_mfma_f32_16x16x128_f8f6f4 v[82:85], v[10:17], v[228:235], v[82:85]
	v_mfma_f32_16x16x128_f8f6f4 v[78:81], v[2:9], v[236:243], v[78:81]
	v_mfma_f32_16x16x128_f8f6f4 v[74:77], v[10:17], v[236:243], v[74:77]
	v_mfma_f32_16x16x128_f8f6f4 v[70:73], v[2:9], v[244:251], v[70:73]
	v_mfma_f32_16x16x128_f8f6f4 v[66:69], v[10:17], v[244:251], v[66:69]
	s_setprio 0
	s_barrier
	s_add_i32 s81, s66, s51
	v_lshl_add_u64 v[200:201], s[46:47], 0, v[162:163]
	s_mov_b32 m0, s81
	ds_read_b128 v[220:223], v213 offset:16384
	ds_read_b128 v[228:231], v213 offset:18432
	ds_read_b128 v[224:227], v214 offset:16384
	ds_read_b128 v[232:235], v214 offset:18432
	ds_read_b128 v[236:239], v213 offset:20480
	ds_read_b128 v[244:247], v213 offset:22528
	ds_read_b128 v[240:243], v214 offset:20480
	ds_read_b128 v[248:251], v214 offset:22528
	global_load_lds_dwordx4 v[200:201], off
	s_add_i32 m0, s81, 0x2000
	s_add_u32 s82, s46, 0x40000
	v_lshl_add_u64 v[202:203], s[46:47], 0, v[164:165]
	s_addc_u32 s83, s47, 0
	s_add_i32 s81, s68, s51
	global_load_lds_dwordx4 v[202:203], off
	s_mov_b32 m0, s81
	s_nop 0
	global_load_lds_dwordx4 v162, s[82:83]
	s_add_i32 m0, s81, 0x2000
	s_nop 0
	global_load_lds_dwordx4 v164, s[82:83]
	s_waitcnt vmcnt(6)
	s_waitcnt lgkmcnt(0)
	s_barrier
	s_setprio 1
	s_waitcnt lgkmcnt(0)
	v_mfma_f32_16x16x128_f8f6f4 v[126:129], v[18:25], v[220:227], v[126:129]
	v_mfma_f32_16x16x128_f8f6f4 v[122:125], v[26:33], v[220:227], v[122:125]
	v_mfma_f32_16x16x128_f8f6f4 v[118:121], v[18:25], v[228:235], v[118:121]
	v_mfma_f32_16x16x128_f8f6f4 v[114:117], v[26:33], v[228:235], v[114:117]
	v_mfma_f32_16x16x128_f8f6f4 v[110:113], v[18:25], v[236:243], v[110:113]
	v_mfma_f32_16x16x128_f8f6f4 v[106:109], v[26:33], v[236:243], v[106:109]
	v_mfma_f32_16x16x128_f8f6f4 v[98:101], v[18:25], v[244:251], v[98:101]
	v_mfma_f32_16x16x128_f8f6f4 v[90:93], v[26:33], v[244:251], v[90:93]
	s_setprio 0
	s_setprio 1
	v_mfma_f32_16x16x128_f8f6f4 v[62:65], v[2:9], v[220:227], v[62:65]
	v_mfma_f32_16x16x128_f8f6f4 v[58:61], v[10:17], v[220:227], v[58:61]
	v_mfma_f32_16x16x128_f8f6f4 v[54:57], v[2:9], v[228:235], v[54:57]
	v_mfma_f32_16x16x128_f8f6f4 v[50:53], v[10:17], v[228:235], v[50:53]
	v_mfma_f32_16x16x128_f8f6f4 v[46:49], v[2:9], v[236:243], v[46:49]
	v_mfma_f32_16x16x128_f8f6f4 v[42:45], v[10:17], v[236:243], v[42:45]
	v_mfma_f32_16x16x128_f8f6f4 v[38:41], v[2:9], v[244:251], v[38:41]
	v_mfma_f32_16x16x128_f8f6f4 v[34:37], v[10:17], v[244:251], v[34:37]
	s_setprio 0
	s_barrier
.Lp7_blk3:
	ds_read_b128 v[2:5], v210 offset:32768
	ds_read_b128 v[6:9], v211 offset:32768
	ds_read_b128 v[10:13], v210 offset:34816
	ds_read_b128 v[14:17], v211 offset:34816
	ds_read_b128 v[18:21], v210 offset:49152
	ds_read_b128 v[22:25], v211 offset:49152
	ds_read_b128 v[26:29], v210 offset:51200
	ds_read_b128 v[30:33], v211 offset:51200
	s_mov_b32 m0, s41
	ds_read_b128 v[220:223], v213 offset:32768
	ds_read_b128 v[228:231], v213 offset:34816
	ds_read_b128 v[224:227], v214 offset:32768
	ds_read_b128 v[232:235], v214 offset:34816
	ds_read_b128 v[236:239], v213 offset:36864
	ds_read_b128 v[244:247], v213 offset:38912
	ds_read_b128 v[240:243], v214 offset:36864
	ds_read_b128 v[248:251], v214 offset:38912
	global_load_lds_dwordx4 v198, s[48:49]
	s_mov_b32 m0, s53
	global_load_lds_dwordx4 v196, s[48:49]
	s_mov_b32 m0, s54
	global_load_lds_dwordx4 v194, s[48:49]
	s_mov_b32 m0, s55
	s_nop 0
	global_load_lds_dwordx4 v192, s[48:49]
	s_waitcnt vmcnt(8)
	s_waitcnt lgkmcnt(0)
	s_barrier
	s_setprio 1
	s_waitcnt lgkmcnt(0)
	v_mfma_f32_16x16x128_f8f6f4 v[158:161], v[2:9], v[220:227], v[158:161]
	v_mfma_f32_16x16x128_f8f6f4 v[154:157], v[10:17], v[220:227], v[154:157]
	v_mfma_f32_16x16x128_f8f6f4 v[150:153], v[2:9], v[228:235], v[150:153]
	v_mfma_f32_16x16x128_f8f6f4 v[146:149], v[10:17], v[228:235], v[146:149]
	v_mfma_f32_16x16x128_f8f6f4 v[142:145], v[2:9], v[236:243], v[142:145]
	v_mfma_f32_16x16x128_f8f6f4 v[138:141], v[10:17], v[236:243], v[138:141]
	v_mfma_f32_16x16x128_f8f6f4 v[134:137], v[2:9], v[244:251], v[134:137]
	v_mfma_f32_16x16x128_f8f6f4 v[130:133], v[10:17], v[244:251], v[130:133]
	s_setprio 0
	s_setprio 1
	v_mfma_f32_16x16x128_f8f6f4 v[102:105], v[18:25], v[220:227], v[102:105]
	v_mfma_f32_16x16x128_f8f6f4 v[94:97], v[26:33], v[220:227], v[94:97]
	v_mfma_f32_16x16x128_f8f6f4 v[86:89], v[18:25], v[228:235], v[86:89]
	v_mfma_f32_16x16x128_f8f6f4 v[82:85], v[26:33], v[228:235], v[82:85]
	v_mfma_f32_16x16x128_f8f6f4 v[78:81], v[18:25], v[236:243], v[78:81]
	v_mfma_f32_16x16x128_f8f6f4 v[74:77], v[26:33], v[236:243], v[74:77]
	v_mfma_f32_16x16x128_f8f6f4 v[70:73], v[18:25], v[244:251], v[70:73]
	v_mfma_f32_16x16x128_f8f6f4 v[66:69], v[26:33], v[244:251], v[66:69]
	s_setprio 0
	s_barrier
	s_add_i32 s48, s70, s51
	v_lshl_add_u64 v[200:201], v[200:201], 0, s[10:11]
	s_mov_b32 m0, s48
	ds_read_b128 v[192:195], v213 offset:49152
	ds_read_b128 v[220:223], v213 offset:51200
	ds_read_b128 v[196:199], v214 offset:49152
	ds_read_b128 v[224:227], v214 offset:51200
	ds_read_b128 v[228:231], v213 offset:53248
	ds_read_b128 v[236:239], v213 offset:55296
	ds_read_b128 v[232:235], v214 offset:53248
	ds_read_b128 v[240:243], v214 offset:55296
	global_load_lds_dwordx4 v[200:201], off
	s_add_i32 m0, s48, 0x2000
	s_add_u32 s46, s46, 0x40080
	v_lshl_add_u64 v[200:201], v[202:203], 0, s[10:11]
	s_addc_u32 s47, s47, 0
	s_add_i32 s48, s72, s51
	global_load_lds_dwordx4 v[200:201], off
	s_mov_b32 m0, s48
	s_nop 0
	global_load_lds_dwordx4 v162, s[46:47]
	s_add_i32 m0, s48, 0x2000
	s_nop 0
	global_load_lds_dwordx4 v164, s[46:47]
	s_waitcnt vmcnt(6)
	s_waitcnt lgkmcnt(0)
	s_barrier
	s_setprio 1
	s_waitcnt lgkmcnt(0)
	v_mfma_f32_16x16x128_f8f6f4 v[126:129], v[2:9], v[192:199], v[126:129]
	v_mfma_f32_16x16x128_f8f6f4 v[122:125], v[10:17], v[192:199], v[122:125]
	v_mfma_f32_16x16x128_f8f6f4 v[118:121], v[2:9], v[220:227], v[118:121]
	v_mfma_f32_16x16x128_f8f6f4 v[114:117], v[10:17], v[220:227], v[114:117]
	v_mfma_f32_16x16x128_f8f6f4 v[110:113], v[2:9], v[228:235], v[110:113]
	v_mfma_f32_16x16x128_f8f6f4 v[106:109], v[10:17], v[228:235], v[106:109]
	v_mfma_f32_16x16x128_f8f6f4 v[98:101], v[2:9], v[236:243], v[98:101]
	v_mfma_f32_16x16x128_f8f6f4 v[90:93], v[10:17], v[236:243], v[90:93]
	s_setprio 0
	s_setprio 1
	v_mfma_f32_16x16x128_f8f6f4 v[62:65], v[18:25], v[192:199], v[62:65]
	v_mfma_f32_16x16x128_f8f6f4 v[58:61], v[26:33], v[192:199], v[58:61]
	v_mfma_f32_16x16x128_f8f6f4 v[54:57], v[18:25], v[220:227], v[54:57]
	v_mfma_f32_16x16x128_f8f6f4 v[50:53], v[26:33], v[220:227], v[50:53]
	v_mfma_f32_16x16x128_f8f6f4 v[46:49], v[18:25], v[228:235], v[46:49]
	v_mfma_f32_16x16x128_f8f6f4 v[42:45], v[26:33], v[228:235], v[42:45]
	v_mfma_f32_16x16x128_f8f6f4 v[38:41], v[18:25], v[236:243], v[38:41]
	v_mfma_f32_16x16x128_f8f6f4 v[34:37], v[26:33], v[236:243], v[34:37]
	s_setprio 0
	s_barrier
	s_add_i32 s43, s43, 2
	s_add_u32 s44, s44, 0x100
	s_addc_u32 s45, s45, 0
	s_cmp_gt_u32 s43, 13
	s_cbranch_scc1 .LBB0_866
